# finish phase: parity-alternating load targets (true 2-deep prefetch), no M set
# baseline (speedup 1.0000x reference)
; __device__ __forceinline__ float siluf_(float x) { return x * __builtin_amdgcn_rcpf(1.f + fexp(-x)); }
; __device__ __forceinline__ float lo16(unsigned u) { return __uint_as_float(u << 16); }
; __device__ void phase_finish(const Params& p, int l, char* smem, int vb, int nvb, int oz) {
;     ...
;     for (int row = rbeg; row < rend; ++row) {
;         bf16_t* ur = U + (size_t)row * LDU;
;         const u32x2 rf = nl[0], rb = nl[1], gf = nl[2], gb = nl[3], zg = nl[4], zr = nl[5];
; #pragma unroll
;         for (int i = 0; i < 6; ++i) nl[i] = nm[i];
;         if (row + 2 < rend) F_LOAD(nm, row + 2)
;         {
;             const float o0 = lo16(gf[0]) + lo16(gb[0]), o1 = hi16(gf[0]) + hi16(gb[0]);
;             const float o2 = lo16(gf[1]) + lo16(gb[1]), o3 = hi16(gf[1]) + hi16(gb[1]);
;             float ss = o0 * o0 + o1 * o1 + o2 * o2 + o3 * o3;
;             ss += __shfl_xor(ss, 1); ss += __shfl_xor(ss, 2); ss += __shfl_xor(ss, 4); ss += __shfl_xor(ss, 8);
;             const float rs = rsqrtf(ss * (1.f / 64.f) + EPS);
;             u32x2 y;
;             y[0] = cvt_pk(o0 * rs * ng.x * siluf_(lo16(zg[0])), o1 * rs * ng.y * siluf_(hi16(zg[0])));
;             y[1] = cvt_pk(o2 * rs * ng.z * siluf_(lo16(zg[1])), o3 * rs * ng.w * siluf_(hi16(zg[1])));
;             st_wt8(ur + C_GZ + lane * 4, y);
;         }
;         {
;             const float o0 = lo16(rf[0]) + lo16(rb[0]), o1 = hi16(rf[0]) + hi16(rb[0]);
;             const float o2 = lo16(rf[1]) + lo16(rb[1]), o3 = hi16(rf[1]) + hi16(rb[1]);
;             float s1 = o0 + o1 + o2 + o3;
;             s1 += __shfl_xor(s1, 1); s1 += __shfl_xor(s1, 2); s1 += __shfl_xor(s1, 4); s1 += __shfl_xor(s1, 8);
;             const float mu = s1 * (1.f / 64.f);
;             const float d0 = o0 - mu, d1 = o1 - mu, d2 = o2 - mu, d3 = o3 - mu;
;             float s2 = d0 * d0 + d1 * d1 + d2 * d2 + d3 * d3;
;             s2 += __shfl_xor(s2, 1); s2 += __shfl_xor(s2, 2); s2 += __shfl_xor(s2, 4); s2 += __shfl_xor(s2, 8);
;             const float rs = rsqrtf(s2 * (1.f / 64.f) + EPS);
;             u32x2 y;
;             y[0] = cvt_pk(d0 * rs * siluf_(lo16(zr[0])), d1 * rs * siluf_(hi16(zr[0])));
;             y[1] = cvt_pk(d2 * rs * siluf_(lo16(zr[1])), d3 * rs * siluf_(hi16(zr[1])));
;             st_wt8(ur + C_RZ + lane * 4, y);
;         }
;     }
.LBB0_245:
	v_lshlrev_b32_e32 v56, 16, v41
	v_and_b32_e32 v57, 0xffff0000, v41
	v_lshlrev_b32_e32 v58, 16, v39
	v_and_b32_e32 v59, 0xffff0000, v39
	v_pk_add_f32 v[56:57], v[58:59], v[56:57]
	v_lshlrev_b32_e32 v58, 16, v40
	v_and_b32_e32 v59, 0xffff0000, v40
	v_lshlrev_b32_e32 v40, 16, v38
	v_and_b32_e32 v41, 0xffff0000, v38
	v_pk_add_f32 v[38:39], v[40:41], v[58:59]
	v_lshlrev_b32_e32 v54, 16, v30
	v_and_b32_e32 v55, 0xffff0000, v30
	v_add_f32_e32 v30, v38, v39
	v_add_f32_e32 v30, v56, v30
	v_add_f32_e32 v30, v57, v30
	v_lshlrev_b32_e32 v50, 16, v33
	v_and_b32_e32 v51, 0xffff0000, v33
	ds_bpermute_b32 v33, v44, v30
	v_mul_f32_e32 v40, 0xbfb8aa3b, v54
	v_mul_f32_e32 v41, 0xbfb8aa3b, v55
	v_lshlrev_b32_e32 v48, 16, v43
	v_and_b32_e32 v49, 0xffff0000, v43
	s_waitcnt lgkmcnt(0)
	v_add_f32_e32 v30, v30, v33
	ds_bpermute_b32 v33, v45, v30
	v_lshlrev_b32_e32 v52, 16, v42
	v_and_b32_e32 v53, 0xffff0000, v42
	v_lshlrev_b32_e32 v42, 16, v32
	v_exp_f32_e32 v40, v40
	s_waitcnt lgkmcnt(0)
	v_add_f32_e32 v30, v30, v33
	ds_bpermute_b32 v58, v46, v30
	v_exp_f32_e32 v41, v41
	v_and_b32_e32 v43, 0xffff0000, v32
	v_pk_add_f32 v[32:33], v[42:43], v[52:53]
	v_add_f32_e32 v40, 1.0, v40
	s_waitcnt lgkmcnt(0)
	v_add_f32_e32 v52, v30, v58
	ds_bpermute_b32 v53, v47, v52
	v_add_f32_e32 v41, 1.0, v41
	v_rcp_f32_e32 v40, v40
	v_rcp_f32_e32 v41, v41
	v_lshlrev_b32_e32 v30, 16, v31
	s_waitcnt lgkmcnt(0)
	v_add_f32_e32 v52, v52, v53
	v_mul_f32_e32 v52, 0x3c800000, v52
	v_pk_mul_f32 v[40:41], v[40:41], v[54:55]
	v_mul_f32_e32 v54, 0xbfb8aa3b, v30
	v_pk_add_f32 v[38:39], v[38:39], v[52:53] op_sel_hi:[1,0] neg_lo:[0,1] neg_hi:[0,1]
	v_pk_add_f32 v[48:49], v[50:51], v[48:49]
	v_pk_mul_f32 v[42:43], v[32:33], v[32:33]
	v_exp_f32_e32 v60, v54
	v_pk_add_f32 v[52:53], v[56:57], v[52:53] op_sel_hi:[1,0] neg_lo:[0,1] neg_hi:[0,1]
	v_pk_mul_f32 v[54:55], v[38:39], v[38:39]
	v_pk_mul_f32 v[50:51], v[48:49], v[48:49]
	v_pk_mul_f32 v[56:57], v[52:53], v[52:53]
	v_mov_b32_e32 v58, v54
	v_mov_b32_e32 v59, v42
	v_mov_b32_e32 v42, v55
	v_pk_add_f32 v[42:43], v[58:59], v[42:43]
	v_mov_b32_e32 v54, v56
	v_mov_b32_e32 v55, v50
	v_pk_add_f32 v[42:43], v[54:55], v[42:43]
	v_mov_b32_e32 v50, v57
	v_pk_add_f32 v[42:43], v[50:51], v[42:43]
	ds_bpermute_b32 v51, v44, v43
	ds_bpermute_b32 v50, v44, v42
	v_lshlrev_b32_e32 v56, 16, v18
	v_and_b32_e32 v57, 0xffff0000, v18
	v_mul_f32_e32 v18, 0xbfb8aa3b, v56
	v_exp_f32_e32 v18, v18
	s_waitcnt lgkmcnt(0)
	v_pk_add_f32 v[42:43], v[42:43], v[50:51]
	ds_bpermute_b32 v51, v45, v43
	ds_bpermute_b32 v50, v45, v42
	v_mul_f32_e32 v58, 0xbfb8aa3b, v57
	v_exp_f32_e32 v59, v58
	v_add_f32_e32 v18, 1.0, v18
	s_mov_b32 s0, 0x3c800000
	s_waitcnt lgkmcnt(0)
	v_pk_add_f32 v[42:43], v[42:43], v[50:51]
	ds_bpermute_b32 v51, v46, v43
	ds_bpermute_b32 v50, v46, v42
	v_rcp_f32_e32 v58, v18
	v_add_f32_e32 v18, 1.0, v59
	v_rcp_f32_e32 v59, v18
	v_and_b32_e32 v31, 0xffff0000, v31
	s_waitcnt lgkmcnt(0)
	v_pk_add_f32 v[42:43], v[42:43], v[50:51]
	ds_bpermute_b32 v51, v47, v43
	ds_bpermute_b32 v50, v47, v42
	v_mul_f32_e32 v55, 0xbfb8aa3b, v31
	v_exp_f32_e32 v55, v55
	v_add_f32_e32 v54, 1.0, v60
	v_rcp_f32_e32 v54, v54
	s_waitcnt lgkmcnt(0)
	v_pk_add_f32 v[42:43], v[42:43], v[50:51]
	v_add_f32_e32 v55, 1.0, v55
	v_pk_fma_f32 v[42:43], v[42:43], s[0:1], v[196:197] op_sel_hi:[1,0,0]
	v_rcp_f32_e32 v55, v55
	v_mul_f32_e32 v18, 0x4b800000, v43
	v_cmp_gt_f32_e32 vcc, s63, v43
	v_lshl_add_u64 v[50:51], s[28:29], 0, v[2:3]
	v_pk_mul_f32 v[30:31], v[54:55], v[30:31]
	v_cndmask_b32_e32 v18, v43, v18, vcc
	v_rsq_f32_e32 v18, v18
	s_mov_b32 s0, 0xb80000
	s_add_i32 s24, s24, 1
	v_pk_mul_f32 v[54:55], v[58:59], v[56:57]
	v_mul_f32_e32 v43, 0x45800000, v18
	v_cndmask_b32_e32 v18, v18, v43, vcc
	v_pk_mul_f32 v[32:33], v[32:33], v[18:19] op_sel_hi:[1,0]
	v_cmp_gt_f32_e32 vcc, s63, v42
	v_pk_mul_f32 v[32:33], v[4:5], v[32:33]
	s_add_u32 s20, s20, 0x1a80
	v_pk_mul_f32 v[32:33], v[40:41], v[32:33]
	v_pk_mul_f32 v[40:41], v[48:49], v[18:19] op_sel_hi:[1,0]
	v_mul_f32_e32 v18, 0x4b800000, v42
	v_cndmask_b32_e32 v18, v42, v18, vcc
	v_pk_mul_f32 v[40:41], v[6:7], v[40:41]
	v_rsq_f32_e32 v18, v18
	v_pk_mul_f32 v[30:31], v[30:31], v[40:41]
	v_cvt_pk_bf16_f32 v32, v32, v33
	v_cvt_pk_bf16_f32 v33, v30, v31
	v_add_co_u32_e64 v30, s[0:1], s0, v50
	s_addc_u32 s21, s21, 0
	s_nop 0
	v_addc_co_u32_e64 v31, s[0:1], 0, v51, s[0:1]
	global_store_dwordx2 v[30:31], v[32:33], off offset:2560 sc1
	v_mul_f32_e32 v30, 0x45800000, v18
	v_cndmask_b32_e32 v18, v18, v30, vcc
	v_lshlrev_b32_e32 v30, 16, v19
	v_and_b32_e32 v31, 0xffff0000, v19
	v_mul_f32_e32 v19, 0xbfb8aa3b, v30
	v_exp_f32_e32 v19, v19
	v_mul_f32_e32 v32, 0xbfb8aa3b, v31
	v_exp_f32_e32 v40, v32
	s_mov_b32 s0, 0xb81000
	v_pk_mul_f32 v[32:33], v[38:39], v[18:19] op_sel_hi:[1,0]
	v_add_f32_e32 v19, 1.0, v19
	v_rcp_f32_e32 v38, v19
	v_add_f32_e32 v19, 1.0, v40
	v_rcp_f32_e32 v39, v19
	v_pk_mul_f32 v[18:19], v[52:53], v[18:19] op_sel_hi:[1,0]
	v_pk_mul_f32 v[32:33], v[54:55], v[32:33]
	s_add_u32 s28, s28, 0x1a80
	v_pk_mul_f32 v[30:31], v[38:39], v[30:31]
	v_cvt_pk_bf16_f32 v32, v32, v33
	v_pk_mul_f32 v[18:19], v[30:31], v[18:19]
	s_addc_u32 s29, s29, 0
	v_cvt_pk_bf16_f32 v33, v18, v19
	v_add_co_u32_e32 v18, vcc, s0, v50
	s_cmp_ge_i32 s24, s2
	s_nop 0
	v_addc_co_u32_e32 v19, vcc, 0, v51, vcc
	global_store_dwordx2 v[18:19], v[32:33], off offset:512 sc1
	s_add_i32 s1, s24, 1
	s_cmp_ge_i32 s1, s2
	s_cbranch_scc1 .Lfin_noload
	s_waitcnt vmcnt(10)
	s_branch .Lfin_w
; __device__ void phase_finish(const Params& p, int l, char* smem, int vb, int nvb, int oz) {
;     ...
;     F_LOAD(nl, rbeg)
;     if (rbeg + 1 < rend) F_LOAD(nm, rbeg + 1)
;     for (int row = rbeg; row < rend; ++row) {
;         bf16_t* ur = U + (size_t)row * LDU;
;         const u32x2 rf = nl[0], rb = nl[1], gf = nl[2], gb = nl[3], zg = nl[4], zr = nl[5];
; #pragma unroll
;         for (int i = 0; i < 6; ++i) nl[i] = nm[i];
;         if (row + 2 < rend) F_LOAD(nm, row + 2)
.Lfin_noload:
	s_waitcnt vmcnt(4)
.Lfin_w:
	s_sub_i32 s1, s24, s3
	s_bitcmp1_b32 s1, 0
	s_cbranch_scc0 .Lfin_from_n0
	v_mov_b64_e32 v[18:19], v[20:21]
	v_mov_b64_e32 v[30:31], v[16:17]
	v_mov_b64_e32 v[32:33], v[10:11]
	v_mov_b64_e32 v[42:43], v[12:13]
	v_mov_b64_e32 v[38:39], v[14:15]
	v_mov_b64_e32 v[40:41], v[8:9]
	s_branch .Lfin_cp_done
.Lfin_from_n0:
	v_mov_b64_e32 v[18:19], v[36:37]
	v_mov_b64_e32 v[30:31], v[34:35]
	v_mov_b64_e32 v[32:33], v[22:23]
	v_mov_b64_e32 v[42:43], v[24:25]
	v_mov_b64_e32 v[38:39], v[26:27]
	v_mov_b64_e32 v[40:41], v[28:29]
.Lfin_cp_done:
	s_cmp_ge_i32 s24, s2
	s_cbranch_scc1 .LBB0_248
.LBB0_246:
	s_add_i32 s0, s24, 2
	s_cmp_ge_i32 s0, s2
	s_cbranch_scc1 .LBB0_245
	s_sub_i32 s1, s24, s3
	s_bitcmp1_b32 s1, 0
	s_cbranch_scc1 .Lfin_ld_n1
	v_lshl_add_u64 v[34:35], s[20:21], 0, v[2:3]
	v_add_co_u32_e32 v36, vcc, 0xb80000, v34
	s_nop 1
	v_addc_co_u32_e32 v37, vcc, 0, v35, vcc
	global_load_dwordx2 v[28:29], v[36:37], off
	global_load_dwordx2 v[26:27], v[36:37], off offset:2048
	global_load_dwordx2 v[24:25], v[36:37], off offset:1024
	global_load_dwordx2 v[22:23], v[36:37], off offset:1536
	v_add_co_u32_e32 v48, vcc, 0xb81000, v34
	s_nop 1
	v_addc_co_u32_e32 v49, vcc, 0, v35, vcc
	global_load_dwordx2 v[34:35], v[36:37], off offset:2560
	s_nop 0
	global_load_dwordx2 v[36:37], v[48:49], off offset:512
	s_branch .LBB0_245
.Lfin_ld_n1:
	v_lshl_add_u64 v[16:17], s[20:21], 0, v[2:3]
	v_add_co_u32_e32 v20, vcc, 0xb80000, v16
	s_nop 1
	v_addc_co_u32_e32 v21, vcc, 0, v17, vcc
	global_load_dwordx2 v[8:9], v[20:21], off
	global_load_dwordx2 v[14:15], v[20:21], off offset:2048
	global_load_dwordx2 v[12:13], v[20:21], off offset:1024
	global_load_dwordx2 v[10:11], v[20:21], off offset:1536
	v_add_co_u32_e32 v48, vcc, 0xb81000, v16
	s_nop 1
	v_addc_co_u32_e32 v49, vcc, 0, v17, vcc
	global_load_dwordx2 v[16:17], v[20:21], off offset:2560
	s_nop 0
	global_load_dwordx2 v[20:21], v[48:49], off offset:512
	s_branch .LBB0_245
